# v71 with the gates epilogue hand-scheduled: in-place chains, software-pipelined over the 8 store groups, each transcendental followed by 2-3 plain ops (replaces gfold)
# baseline (speedup 1.0000x reference)
; __device__ __forceinline__ float fsigmoid(float x) { return __builtin_amdgcn_rcpf(1.0f + __builtin_amdgcn_exp2f(-1.44269504f * x)); }
;     __device__ __forceinline__ void operator()(AccRef acc, const GUnit& u, int wr, int wc, int fr, int fq) const {
;         const int pm = u.x0, pn = u.x1; unsigned char* base = (pn < 8 ? GZF : GZS) + (size_t)(pm * 256 + wr * 64 + fr) * D + (pn & 7) * 256 + wc * 64 + 16 * fq;
; #pragma unroll
;         for (int ai = 0; ai < 2; ++ai)
; #pragma unroll
;             for (int m = 0; m < 4; ++m) { u32x4 w;
; #pragma unroll
;                 for (int bj = 0; bj < 2; ++bj)
; #pragma unroll
;                     for (int n = 0; n < 2; ++n) { const f32x4 v = acc[ai][bj][m][n]; w[bj * 2 + n] = pk4_u8(fsigmoid(v[0] * W8_INV), fsigmoid(v[1] * W8_INV), fsigmoid(v[2] * W8_INV), fsigmoid(v[3] * W8_INV)); }
;                 *(u32x4*)(base + (size_t)(ai * 128 + m * 16) * D) = w; }
;     }
.LBB0_431:
	s_nop 15
	s_nop 7
	v_lshl_add_u32 v2, s8, 8, v190
	s_cmp_lt_i32 s73, 8
	v_ashrrev_i32_e32 v3, 31, v2
	s_cselect_b32 s25, s41, s59
	s_cselect_b32 s24, s40, s53
	v_lshlrev_b64 v[2:3], 11, v[2:3]
	s_lshl_b32 s8, s73, 8
	v_lshl_add_u64 v[2:3], s[24:25], 0, v[2:3]
	s_and_b32 s8, s8, 0x700
	v_lshl_add_u64 v[2:3], v[2:3], 0, s[8:9]
	v_lshl_add_u64 v[2:3], v[2:3], 0, s[14:15]
	v_lshl_add_u64 v[2:3], v[2:3], 0, v[162:163]
	v_mul_f32_e32 v158, 0xbcb8aa3b, v158
	v_mul_f32_e32 v159, 0xbcb8aa3b, v159
	v_mul_f32_e32 v160, 0xbcb8aa3b, v160
	v_mul_f32_e32 v161, 0xbcb8aa3b, v161
	v_mul_f32_e32 v154, 0xbcb8aa3b, v154
	v_mul_f32_e32 v155, 0xbcb8aa3b, v155
	v_mul_f32_e32 v156, 0xbcb8aa3b, v156
	v_mul_f32_e32 v157, 0xbcb8aa3b, v157
	v_mul_f32_e32 v150, 0xbcb8aa3b, v150
	v_mul_f32_e32 v151, 0xbcb8aa3b, v151
	v_mul_f32_e32 v152, 0xbcb8aa3b, v152
	v_mul_f32_e32 v153, 0xbcb8aa3b, v153
	v_mul_f32_e32 v146, 0xbcb8aa3b, v146
	v_mul_f32_e32 v147, 0xbcb8aa3b, v147
	v_mul_f32_e32 v148, 0xbcb8aa3b, v148
	v_mul_f32_e32 v149, 0xbcb8aa3b, v149
	v_exp_f32_e32 v158, v158
	v_mul_f32_e32 v142, 0xbcb8aa3b, v142
	v_exp_f32_e32 v159, v159
	v_mul_f32_e32 v143, 0xbcb8aa3b, v143
	v_exp_f32_e32 v160, v160
	v_mul_f32_e32 v144, 0xbcb8aa3b, v144
	v_exp_f32_e32 v161, v161
	v_mul_f32_e32 v145, 0xbcb8aa3b, v145
	v_exp_f32_e32 v154, v154
	v_mul_f32_e32 v138, 0xbcb8aa3b, v138
	v_exp_f32_e32 v155, v155
	v_mul_f32_e32 v139, 0xbcb8aa3b, v139
	v_exp_f32_e32 v156, v156
	v_mul_f32_e32 v140, 0xbcb8aa3b, v140
	v_exp_f32_e32 v157, v157
	v_mul_f32_e32 v141, 0xbcb8aa3b, v141
	v_exp_f32_e32 v150, v150
	v_mul_f32_e32 v134, 0xbcb8aa3b, v134
	v_exp_f32_e32 v151, v151
	v_mul_f32_e32 v135, 0xbcb8aa3b, v135
	v_exp_f32_e32 v152, v152
	v_mul_f32_e32 v136, 0xbcb8aa3b, v136
	v_exp_f32_e32 v153, v153
	v_mul_f32_e32 v137, 0xbcb8aa3b, v137
	v_exp_f32_e32 v146, v146
	v_mul_f32_e32 v130, 0xbcb8aa3b, v130
	v_exp_f32_e32 v147, v147
	v_mul_f32_e32 v131, 0xbcb8aa3b, v131
	v_exp_f32_e32 v148, v148
	v_mul_f32_e32 v132, 0xbcb8aa3b, v132
	v_exp_f32_e32 v149, v149
	v_mul_f32_e32 v133, 0xbcb8aa3b, v133
	v_add_f32_e32 v158, 1.0, v158
	v_add_f32_e32 v159, 1.0, v159
	v_add_f32_e32 v160, 1.0, v160
	v_add_f32_e32 v161, 1.0, v161
	v_add_f32_e32 v154, 1.0, v154
	v_add_f32_e32 v155, 1.0, v155
	v_add_f32_e32 v156, 1.0, v156
	v_add_f32_e32 v157, 1.0, v157
	v_add_f32_e32 v150, 1.0, v150
	v_add_f32_e32 v151, 1.0, v151
	v_add_f32_e32 v152, 1.0, v152
	v_add_f32_e32 v153, 1.0, v153
	v_add_f32_e32 v146, 1.0, v146
	v_add_f32_e32 v147, 1.0, v147
	v_add_f32_e32 v148, 1.0, v148
	v_add_f32_e32 v149, 1.0, v149
	v_exp_f32_e32 v142, v142
	v_mul_f32_e32 v126, 0xbcb8aa3b, v126
	v_exp_f32_e32 v143, v143
	v_mul_f32_e32 v127, 0xbcb8aa3b, v127
	v_exp_f32_e32 v144, v144
	v_mul_f32_e32 v128, 0xbcb8aa3b, v128
	v_exp_f32_e32 v145, v145
	v_mul_f32_e32 v129, 0xbcb8aa3b, v129
	v_exp_f32_e32 v138, v138
	v_mul_f32_e32 v122, 0xbcb8aa3b, v122
	v_exp_f32_e32 v139, v139
	v_mul_f32_e32 v123, 0xbcb8aa3b, v123
	v_exp_f32_e32 v140, v140
	v_mul_f32_e32 v124, 0xbcb8aa3b, v124
	v_exp_f32_e32 v141, v141
	v_mul_f32_e32 v125, 0xbcb8aa3b, v125
	v_exp_f32_e32 v134, v134
	v_mul_f32_e32 v118, 0xbcb8aa3b, v118
	v_exp_f32_e32 v135, v135
	v_mul_f32_e32 v119, 0xbcb8aa3b, v119
	v_exp_f32_e32 v136, v136
	v_mul_f32_e32 v120, 0xbcb8aa3b, v120
	v_exp_f32_e32 v137, v137
	v_mul_f32_e32 v121, 0xbcb8aa3b, v121
	v_exp_f32_e32 v130, v130
	v_mul_f32_e32 v114, 0xbcb8aa3b, v114
	v_exp_f32_e32 v131, v131
	v_mul_f32_e32 v115, 0xbcb8aa3b, v115
	v_exp_f32_e32 v132, v132
	v_mul_f32_e32 v116, 0xbcb8aa3b, v116
	v_exp_f32_e32 v133, v133
	v_mul_f32_e32 v117, 0xbcb8aa3b, v117
	v_rcp_f32_e32 v158, v158
	v_add_f32_e32 v142, 1.0, v142
	v_rcp_f32_e32 v159, v159
	v_add_f32_e32 v143, 1.0, v143
	v_rcp_f32_e32 v160, v160
	v_add_f32_e32 v144, 1.0, v144
	v_rcp_f32_e32 v161, v161
	v_add_f32_e32 v145, 1.0, v145
	v_rcp_f32_e32 v154, v154
	v_add_f32_e32 v138, 1.0, v138
	v_rcp_f32_e32 v155, v155
	v_add_f32_e32 v139, 1.0, v139
	v_rcp_f32_e32 v156, v156
	v_add_f32_e32 v140, 1.0, v140
	v_rcp_f32_e32 v157, v157
	v_add_f32_e32 v141, 1.0, v141
	v_rcp_f32_e32 v150, v150
	v_add_f32_e32 v134, 1.0, v134
	v_rcp_f32_e32 v151, v151
	v_add_f32_e32 v135, 1.0, v135
	v_rcp_f32_e32 v152, v152
	v_add_f32_e32 v136, 1.0, v136
	v_rcp_f32_e32 v153, v153
	v_add_f32_e32 v137, 1.0, v137
	v_rcp_f32_e32 v146, v146
	v_add_f32_e32 v130, 1.0, v130
	v_rcp_f32_e32 v147, v147
	v_add_f32_e32 v131, 1.0, v131
	v_rcp_f32_e32 v148, v148
	v_add_f32_e32 v132, 1.0, v132
	v_rcp_f32_e32 v149, v149
	v_add_f32_e32 v133, 1.0, v133
	v_exp_f32_e32 v126, v126
	v_mul_f32_e32 v110, 0xbcb8aa3b, v110
	v_fmamk_f32 v158, v158, 0x437f0000, v196
	v_exp_f32_e32 v127, v127
	v_mul_f32_e32 v111, 0xbcb8aa3b, v111
	v_fmamk_f32 v159, v159, 0x437f0000, v196
	v_exp_f32_e32 v128, v128
	v_mul_f32_e32 v112, 0xbcb8aa3b, v112
	v_fmamk_f32 v160, v160, 0x437f0000, v196
	v_exp_f32_e32 v129, v129
	v_mul_f32_e32 v113, 0xbcb8aa3b, v113
	v_fmamk_f32 v161, v161, 0x437f0000, v196
	v_exp_f32_e32 v122, v122
	v_mul_f32_e32 v106, 0xbcb8aa3b, v106
	v_fmamk_f32 v154, v154, 0x437f0000, v196
	v_exp_f32_e32 v123, v123
	v_mul_f32_e32 v107, 0xbcb8aa3b, v107
	v_fmamk_f32 v155, v155, 0x437f0000, v196
	v_exp_f32_e32 v124, v124
	v_mul_f32_e32 v108, 0xbcb8aa3b, v108
	v_fmamk_f32 v156, v156, 0x437f0000, v196
	v_exp_f32_e32 v125, v125
	v_mul_f32_e32 v109, 0xbcb8aa3b, v109
	v_fmamk_f32 v157, v157, 0x437f0000, v196
	v_exp_f32_e32 v118, v118
	v_mul_f32_e32 v102, 0xbcb8aa3b, v102
	v_fmamk_f32 v150, v150, 0x437f0000, v196
	v_exp_f32_e32 v119, v119
	v_mul_f32_e32 v103, 0xbcb8aa3b, v103
	v_fmamk_f32 v151, v151, 0x437f0000, v196
	v_exp_f32_e32 v120, v120
	v_mul_f32_e32 v104, 0xbcb8aa3b, v104
	v_fmamk_f32 v152, v152, 0x437f0000, v196
; __device__ __forceinline__ float fsigmoid(float x) { return __builtin_amdgcn_rcpf(1.0f + __builtin_amdgcn_exp2f(-1.44269504f * x)); }
; __device__ __forceinline__ unsigned pk4_u8(float a, float b, float c, float d) {
;     const unsigned ya = __builtin_bit_cast(unsigned, a * 255.0f + 8388608.0f), yb = __builtin_bit_cast(unsigned, b * 255.0f + 8388608.0f), yc = __builtin_bit_cast(unsigned, c * 255.0f + 8388608.0f), yd = __builtin_bit_cast(unsigned, d * 255.0f + 8388608.0f);
;     const unsigned w01 = __builtin_amdgcn_perm(yb, ya, 0x0c0c0400u), w23 = __builtin_amdgcn_perm(yd, yc, 0x0c0c0400u);
;     return __builtin_amdgcn_perm(w23, w01, 0x05040100u); }
;     __device__ __forceinline__ void operator()(AccRef acc, const GUnit& u, int wr, int wc, int fr, int fq) const {
;     ...
;             for (int m = 0; m < 4; ++m) { u32x4 w;
; #pragma unroll
;                 for (int bj = 0; bj < 2; ++bj)
; #pragma unroll
;                     for (int n = 0; n < 2; ++n) { const f32x4 v = acc[ai][bj][m][n]; w[bj * 2 + n] = pk4_u8(fsigmoid(v[0] * W8_INV), fsigmoid(v[1] * W8_INV), fsigmoid(v[2] * W8_INV), fsigmoid(v[3] * W8_INV)); }
;                 *(u32x4*)(base + (size_t)(ai * 128 + m * 16) * D) = w; }
	v_exp_f32_e32 v121, v121
	v_mul_f32_e32 v105, 0xbcb8aa3b, v105
	v_fmamk_f32 v153, v153, 0x437f0000, v196
	v_exp_f32_e32 v114, v114
	v_mul_f32_e32 v98, 0xbcb8aa3b, v98
	v_fmamk_f32 v146, v146, 0x437f0000, v196
	v_exp_f32_e32 v115, v115
	v_mul_f32_e32 v99, 0xbcb8aa3b, v99
	v_fmamk_f32 v147, v147, 0x437f0000, v196
	v_exp_f32_e32 v116, v116
	v_mul_f32_e32 v100, 0xbcb8aa3b, v100
	v_fmamk_f32 v148, v148, 0x437f0000, v196
	v_exp_f32_e32 v117, v117
	v_mul_f32_e32 v101, 0xbcb8aa3b, v101
	v_fmamk_f32 v149, v149, 0x437f0000, v196
	v_rcp_f32_e32 v142, v142
	v_add_f32_e32 v126, 1.0, v126
	v_rcp_f32_e32 v143, v143
	v_add_f32_e32 v127, 1.0, v127
	v_rcp_f32_e32 v144, v144
	v_add_f32_e32 v128, 1.0, v128
	v_rcp_f32_e32 v145, v145
	v_add_f32_e32 v129, 1.0, v129
	v_rcp_f32_e32 v138, v138
	v_add_f32_e32 v122, 1.0, v122
	v_rcp_f32_e32 v139, v139
	v_add_f32_e32 v123, 1.0, v123
	v_rcp_f32_e32 v140, v140
	v_add_f32_e32 v124, 1.0, v124
	v_rcp_f32_e32 v141, v141
	v_add_f32_e32 v125, 1.0, v125
	v_rcp_f32_e32 v134, v134
	v_add_f32_e32 v118, 1.0, v118
	v_rcp_f32_e32 v135, v135
	v_add_f32_e32 v119, 1.0, v119
	v_rcp_f32_e32 v136, v136
	v_add_f32_e32 v120, 1.0, v120
	v_rcp_f32_e32 v137, v137
	v_add_f32_e32 v121, 1.0, v121
	v_rcp_f32_e32 v130, v130
	v_add_f32_e32 v114, 1.0, v114
	v_rcp_f32_e32 v131, v131
	v_add_f32_e32 v115, 1.0, v115
	v_rcp_f32_e32 v132, v132
	v_add_f32_e32 v116, 1.0, v116
	v_rcp_f32_e32 v133, v133
	v_add_f32_e32 v117, 1.0, v117
	v_exp_f32_e32 v110, v110
	v_mul_f32_e32 v94, 0xbcb8aa3b, v94
	v_fmamk_f32 v142, v142, 0x437f0000, v196
	v_exp_f32_e32 v111, v111
	v_mul_f32_e32 v95, 0xbcb8aa3b, v95
	v_fmamk_f32 v143, v143, 0x437f0000, v196
	v_exp_f32_e32 v112, v112
	v_mul_f32_e32 v96, 0xbcb8aa3b, v96
	v_fmamk_f32 v144, v144, 0x437f0000, v196
	v_exp_f32_e32 v113, v113
	v_mul_f32_e32 v97, 0xbcb8aa3b, v97
	v_fmamk_f32 v145, v145, 0x437f0000, v196
	v_exp_f32_e32 v106, v106
	v_mul_f32_e32 v90, 0xbcb8aa3b, v90
	v_fmamk_f32 v138, v138, 0x437f0000, v196
	v_exp_f32_e32 v107, v107
	v_mul_f32_e32 v91, 0xbcb8aa3b, v91
	v_fmamk_f32 v139, v139, 0x437f0000, v196
	v_exp_f32_e32 v108, v108
	v_mul_f32_e32 v92, 0xbcb8aa3b, v92
	v_fmamk_f32 v140, v140, 0x437f0000, v196
	v_exp_f32_e32 v109, v109
	v_mul_f32_e32 v93, 0xbcb8aa3b, v93
	v_fmamk_f32 v141, v141, 0x437f0000, v196
	v_exp_f32_e32 v102, v102
	v_mul_f32_e32 v86, 0xbcb8aa3b, v86
	v_fmamk_f32 v134, v134, 0x437f0000, v196
	v_exp_f32_e32 v103, v103
	v_mul_f32_e32 v87, 0xbcb8aa3b, v87
	v_fmamk_f32 v135, v135, 0x437f0000, v196
	v_exp_f32_e32 v104, v104
	v_mul_f32_e32 v88, 0xbcb8aa3b, v88
	v_fmamk_f32 v136, v136, 0x437f0000, v196
	v_exp_f32_e32 v105, v105
	v_mul_f32_e32 v89, 0xbcb8aa3b, v89
	v_fmamk_f32 v137, v137, 0x437f0000, v196
	v_exp_f32_e32 v98, v98
	v_mul_f32_e32 v82, 0xbcb8aa3b, v82
	v_fmamk_f32 v130, v130, 0x437f0000, v196
	v_exp_f32_e32 v99, v99
	v_mul_f32_e32 v83, 0xbcb8aa3b, v83
	v_fmamk_f32 v131, v131, 0x437f0000, v196
	v_exp_f32_e32 v100, v100
	v_mul_f32_e32 v84, 0xbcb8aa3b, v84
	v_fmamk_f32 v132, v132, 0x437f0000, v196
	v_exp_f32_e32 v101, v101
	v_mul_f32_e32 v85, 0xbcb8aa3b, v85
	v_fmamk_f32 v133, v133, 0x437f0000, v196
	v_rcp_f32_e32 v126, v126
	v_add_f32_e32 v110, 1.0, v110
	v_perm_b32 v158, v159, v158, s67
	v_rcp_f32_e32 v127, v127
	v_add_f32_e32 v111, 1.0, v111
	v_perm_b32 v160, v161, v160, s67
	v_rcp_f32_e32 v128, v128
	v_add_f32_e32 v112, 1.0, v112
	v_perm_b32 v4, v160, v158, s68
	v_rcp_f32_e32 v129, v129
	v_add_f32_e32 v113, 1.0, v113
	v_perm_b32 v154, v155, v154, s67
	v_rcp_f32_e32 v122, v122
	v_add_f32_e32 v106, 1.0, v106
	v_perm_b32 v156, v157, v156, s67
	v_rcp_f32_e32 v123, v123
	v_add_f32_e32 v107, 1.0, v107
	v_perm_b32 v5, v156, v154, s68
	v_rcp_f32_e32 v124, v124
	v_add_f32_e32 v108, 1.0, v108
	v_perm_b32 v150, v151, v150, s67
	v_rcp_f32_e32 v125, v125
	v_add_f32_e32 v109, 1.0, v109
	v_perm_b32 v152, v153, v152, s67
	v_rcp_f32_e32 v118, v118
	v_add_f32_e32 v102, 1.0, v102
	v_perm_b32 v6, v152, v150, s68
	v_rcp_f32_e32 v119, v119
	v_add_f32_e32 v103, 1.0, v103
	v_perm_b32 v146, v147, v146, s67
	v_rcp_f32_e32 v120, v120
	v_add_f32_e32 v104, 1.0, v104
	v_perm_b32 v148, v149, v148, s67
	v_rcp_f32_e32 v121, v121
	v_add_f32_e32 v105, 1.0, v105
	v_perm_b32 v7, v148, v146, s68
	v_rcp_f32_e32 v114, v114
	v_add_f32_e32 v98, 1.0, v98
	v_rcp_f32_e32 v115, v115
	v_add_f32_e32 v99, 1.0, v99
	v_rcp_f32_e32 v116, v116
	v_add_f32_e32 v100, 1.0, v100
	v_rcp_f32_e32 v117, v117
	v_add_f32_e32 v101, 1.0, v101
	global_store_dwordx4 v[2:3], v[4:7], off
	v_exp_f32_e32 v94, v94
	v_mul_f32_e32 v78, 0xbcb8aa3b, v78
	v_fmamk_f32 v126, v126, 0x437f0000, v196
	v_exp_f32_e32 v95, v95
	v_mul_f32_e32 v79, 0xbcb8aa3b, v79
	v_fmamk_f32 v127, v127, 0x437f0000, v196
	v_exp_f32_e32 v96, v96
	v_mul_f32_e32 v80, 0xbcb8aa3b, v80
	v_fmamk_f32 v128, v128, 0x437f0000, v196
	v_exp_f32_e32 v97, v97
	v_mul_f32_e32 v81, 0xbcb8aa3b, v81
	v_fmamk_f32 v129, v129, 0x437f0000, v196
	v_exp_f32_e32 v90, v90
	v_mul_f32_e32 v74, 0xbcb8aa3b, v74
	v_fmamk_f32 v122, v122, 0x437f0000, v196
	v_exp_f32_e32 v91, v91
	v_mul_f32_e32 v75, 0xbcb8aa3b, v75
	v_fmamk_f32 v123, v123, 0x437f0000, v196
	v_exp_f32_e32 v92, v92
	v_mul_f32_e32 v76, 0xbcb8aa3b, v76
	v_fmamk_f32 v124, v124, 0x437f0000, v196
	v_exp_f32_e32 v93, v93
	v_mul_f32_e32 v77, 0xbcb8aa3b, v77
	v_fmamk_f32 v125, v125, 0x437f0000, v196
	v_exp_f32_e32 v86, v86
	v_mul_f32_e32 v70, 0xbcb8aa3b, v70
	v_fmamk_f32 v118, v118, 0x437f0000, v196
	v_exp_f32_e32 v87, v87
	v_mul_f32_e32 v71, 0xbcb8aa3b, v71
	v_fmamk_f32 v119, v119, 0x437f0000, v196
	v_exp_f32_e32 v88, v88
	v_mul_f32_e32 v72, 0xbcb8aa3b, v72
	v_fmamk_f32 v120, v120, 0x437f0000, v196
	v_exp_f32_e32 v89, v89
	v_mul_f32_e32 v73, 0xbcb8aa3b, v73
; __device__ __forceinline__ float fsigmoid(float x) { return __builtin_amdgcn_rcpf(1.0f + __builtin_amdgcn_exp2f(-1.44269504f * x)); }
; __device__ __forceinline__ unsigned pk4_u8(float a, float b, float c, float d) {
;     const unsigned ya = __builtin_bit_cast(unsigned, a * 255.0f + 8388608.0f), yb = __builtin_bit_cast(unsigned, b * 255.0f + 8388608.0f), yc = __builtin_bit_cast(unsigned, c * 255.0f + 8388608.0f), yd = __builtin_bit_cast(unsigned, d * 255.0f + 8388608.0f);
;     const unsigned w01 = __builtin_amdgcn_perm(yb, ya, 0x0c0c0400u), w23 = __builtin_amdgcn_perm(yd, yc, 0x0c0c0400u);
;     return __builtin_amdgcn_perm(w23, w01, 0x05040100u); }
;     __device__ __forceinline__ void operator()(AccRef acc, const GUnit& u, int wr, int wc, int fr, int fq) const {
;     ...
;             for (int m = 0; m < 4; ++m) { u32x4 w;
; #pragma unroll
;                 for (int bj = 0; bj < 2; ++bj)
; #pragma unroll
;                     for (int n = 0; n < 2; ++n) { const f32x4 v = acc[ai][bj][m][n]; w[bj * 2 + n] = pk4_u8(fsigmoid(v[0] * W8_INV), fsigmoid(v[1] * W8_INV), fsigmoid(v[2] * W8_INV), fsigmoid(v[3] * W8_INV)); }
;                 *(u32x4*)(base + (size_t)(ai * 128 + m * 16) * D) = w; }
	v_fmamk_f32 v121, v121, 0x437f0000, v196
	v_exp_f32_e32 v82, v82
	v_mul_f32_e32 v66, 0xbcb8aa3b, v66
	v_fmamk_f32 v114, v114, 0x437f0000, v196
	v_exp_f32_e32 v83, v83
	v_mul_f32_e32 v67, 0xbcb8aa3b, v67
	v_fmamk_f32 v115, v115, 0x437f0000, v196
	v_exp_f32_e32 v84, v84
	v_mul_f32_e32 v68, 0xbcb8aa3b, v68
	v_fmamk_f32 v116, v116, 0x437f0000, v196
	v_exp_f32_e32 v85, v85
	v_mul_f32_e32 v69, 0xbcb8aa3b, v69
	v_fmamk_f32 v117, v117, 0x437f0000, v196
	v_rcp_f32_e32 v110, v110
	v_add_f32_e32 v94, 1.0, v94
	v_perm_b32 v142, v143, v142, s67
	v_rcp_f32_e32 v111, v111
	v_add_f32_e32 v95, 1.0, v95
	v_perm_b32 v144, v145, v144, s67
	v_rcp_f32_e32 v112, v112
	v_add_f32_e32 v96, 1.0, v96
	v_perm_b32 v10, v144, v142, s68
	v_rcp_f32_e32 v113, v113
	v_add_f32_e32 v97, 1.0, v97
	v_perm_b32 v138, v139, v138, s67
	v_rcp_f32_e32 v106, v106
	v_add_f32_e32 v90, 1.0, v90
	v_perm_b32 v140, v141, v140, s67
	v_rcp_f32_e32 v107, v107
	v_add_f32_e32 v91, 1.0, v91
	v_perm_b32 v11, v140, v138, s68
	v_rcp_f32_e32 v108, v108
	v_add_f32_e32 v92, 1.0, v92
	v_perm_b32 v134, v135, v134, s67
	v_rcp_f32_e32 v109, v109
	v_add_f32_e32 v93, 1.0, v93
	v_perm_b32 v136, v137, v136, s67
	v_rcp_f32_e32 v102, v102
	v_add_f32_e32 v86, 1.0, v86
	v_perm_b32 v12, v136, v134, s68
	v_rcp_f32_e32 v103, v103
	v_add_f32_e32 v87, 1.0, v87
	v_perm_b32 v130, v131, v130, s67
	v_rcp_f32_e32 v104, v104
	v_add_f32_e32 v88, 1.0, v88
	v_perm_b32 v132, v133, v132, s67
	v_rcp_f32_e32 v105, v105
	v_add_f32_e32 v89, 1.0, v89
	v_perm_b32 v13, v132, v130, s68
	v_rcp_f32_e32 v98, v98
	v_add_f32_e32 v82, 1.0, v82
	v_add_co_u32_e32 v8, vcc, s63, v2
	v_rcp_f32_e32 v99, v99
	v_add_f32_e32 v83, 1.0, v83
	v_rcp_f32_e32 v100, v100
	v_add_f32_e32 v84, 1.0, v84
	v_addc_co_u32_e32 v9, vcc, 0, v3, vcc
	v_rcp_f32_e32 v101, v101
	v_add_f32_e32 v85, 1.0, v85
	global_store_dwordx4 v[8:9], v[10:13], off
	v_exp_f32_e32 v78, v78
	v_mul_f32_e32 v62, 0xbcb8aa3b, v62
	v_fmamk_f32 v110, v110, 0x437f0000, v196
	v_exp_f32_e32 v79, v79
	v_mul_f32_e32 v63, 0xbcb8aa3b, v63
	v_fmamk_f32 v111, v111, 0x437f0000, v196
	v_exp_f32_e32 v80, v80
	v_mul_f32_e32 v64, 0xbcb8aa3b, v64
	v_fmamk_f32 v112, v112, 0x437f0000, v196
	v_exp_f32_e32 v81, v81
	v_mul_f32_e32 v65, 0xbcb8aa3b, v65
	v_fmamk_f32 v113, v113, 0x437f0000, v196
	v_exp_f32_e32 v74, v74
	v_mul_f32_e32 v58, 0xbcb8aa3b, v58
	v_fmamk_f32 v106, v106, 0x437f0000, v196
	v_exp_f32_e32 v75, v75
	v_mul_f32_e32 v59, 0xbcb8aa3b, v59
	v_fmamk_f32 v107, v107, 0x437f0000, v196
	v_exp_f32_e32 v76, v76
	v_mul_f32_e32 v60, 0xbcb8aa3b, v60
	v_fmamk_f32 v108, v108, 0x437f0000, v196
	v_exp_f32_e32 v77, v77
	v_mul_f32_e32 v61, 0xbcb8aa3b, v61
	v_fmamk_f32 v109, v109, 0x437f0000, v196
	v_exp_f32_e32 v70, v70
	v_mul_f32_e32 v54, 0xbcb8aa3b, v54
	v_fmamk_f32 v102, v102, 0x437f0000, v196
	v_exp_f32_e32 v71, v71
	v_mul_f32_e32 v55, 0xbcb8aa3b, v55
	v_fmamk_f32 v103, v103, 0x437f0000, v196
	v_exp_f32_e32 v72, v72
	v_mul_f32_e32 v56, 0xbcb8aa3b, v56
	v_fmamk_f32 v104, v104, 0x437f0000, v196
	v_exp_f32_e32 v73, v73
	v_mul_f32_e32 v57, 0xbcb8aa3b, v57
	v_fmamk_f32 v105, v105, 0x437f0000, v196
	v_exp_f32_e32 v66, v66
	v_mul_f32_e32 v50, 0xbcb8aa3b, v50
	v_fmamk_f32 v98, v98, 0x437f0000, v196
	v_exp_f32_e32 v67, v67
	v_mul_f32_e32 v51, 0xbcb8aa3b, v51
	v_fmamk_f32 v99, v99, 0x437f0000, v196
	v_exp_f32_e32 v68, v68
	v_mul_f32_e32 v52, 0xbcb8aa3b, v52
	v_fmamk_f32 v100, v100, 0x437f0000, v196
	v_exp_f32_e32 v69, v69
	v_mul_f32_e32 v53, 0xbcb8aa3b, v53
	v_fmamk_f32 v101, v101, 0x437f0000, v196
	v_rcp_f32_e32 v94, v94
	v_add_f32_e32 v78, 1.0, v78
	v_perm_b32 v126, v127, v126, s67
	v_rcp_f32_e32 v95, v95
	v_add_f32_e32 v79, 1.0, v79
	v_perm_b32 v128, v129, v128, s67
	v_rcp_f32_e32 v96, v96
	v_add_f32_e32 v80, 1.0, v80
	v_perm_b32 v4, v128, v126, s68
	v_rcp_f32_e32 v97, v97
	v_add_f32_e32 v81, 1.0, v81
	v_perm_b32 v122, v123, v122, s67
	v_rcp_f32_e32 v90, v90
	v_add_f32_e32 v74, 1.0, v74
	v_perm_b32 v124, v125, v124, s67
	v_rcp_f32_e32 v91, v91
	v_add_f32_e32 v75, 1.0, v75
	v_perm_b32 v5, v124, v122, s68
	v_rcp_f32_e32 v92, v92
	v_add_f32_e32 v76, 1.0, v76
	v_perm_b32 v118, v119, v118, s67
	v_rcp_f32_e32 v93, v93
	v_add_f32_e32 v77, 1.0, v77
	v_perm_b32 v120, v121, v120, s67
	v_rcp_f32_e32 v86, v86
	v_add_f32_e32 v70, 1.0, v70
	v_perm_b32 v6, v120, v118, s68
	v_rcp_f32_e32 v87, v87
	v_add_f32_e32 v71, 1.0, v71
	v_perm_b32 v114, v115, v114, s67
	v_rcp_f32_e32 v88, v88
	v_add_f32_e32 v72, 1.0, v72
	v_perm_b32 v116, v117, v116, s67
	v_rcp_f32_e32 v89, v89
	v_add_f32_e32 v73, 1.0, v73
	v_perm_b32 v7, v116, v114, s68
	v_rcp_f32_e32 v82, v82
	v_add_f32_e32 v66, 1.0, v66
	v_add_co_u32_e32 v8, vcc, s52, v2
	v_rcp_f32_e32 v83, v83
	v_add_f32_e32 v67, 1.0, v67
	v_rcp_f32_e32 v84, v84
	v_add_f32_e32 v68, 1.0, v68
	v_addc_co_u32_e32 v9, vcc, 0, v3, vcc
	v_rcp_f32_e32 v85, v85
	v_add_f32_e32 v69, 1.0, v69
	global_store_dwordx4 v[8:9], v[4:7], off
	v_exp_f32_e32 v62, v62
	v_mul_f32_e32 v46, 0xbcb8aa3b, v46
	v_fmamk_f32 v94, v94, 0x437f0000, v196
	v_exp_f32_e32 v63, v63
	v_mul_f32_e32 v47, 0xbcb8aa3b, v47
	v_fmamk_f32 v95, v95, 0x437f0000, v196
	v_exp_f32_e32 v64, v64
	v_mul_f32_e32 v48, 0xbcb8aa3b, v48
	v_fmamk_f32 v96, v96, 0x437f0000, v196
	v_exp_f32_e32 v65, v65
	v_mul_f32_e32 v49, 0xbcb8aa3b, v49
	v_fmamk_f32 v97, v97, 0x437f0000, v196
	v_exp_f32_e32 v58, v58
	v_mul_f32_e32 v42, 0xbcb8aa3b, v42
	v_fmamk_f32 v90, v90, 0x437f0000, v196
	v_exp_f32_e32 v59, v59
	v_mul_f32_e32 v43, 0xbcb8aa3b, v43
	v_fmamk_f32 v91, v91, 0x437f0000, v196
	v_exp_f32_e32 v60, v60
	v_mul_f32_e32 v44, 0xbcb8aa3b, v44
	v_fmamk_f32 v92, v92, 0x437f0000, v196
	v_exp_f32_e32 v61, v61
	v_mul_f32_e32 v45, 0xbcb8aa3b, v45
	v_fmamk_f32 v93, v93, 0x437f0000, v196
; __device__ __forceinline__ float fsigmoid(float x) { return __builtin_amdgcn_rcpf(1.0f + __builtin_amdgcn_exp2f(-1.44269504f * x)); }
; __device__ __forceinline__ unsigned pk4_u8(float a, float b, float c, float d) {
;     const unsigned ya = __builtin_bit_cast(unsigned, a * 255.0f + 8388608.0f), yb = __builtin_bit_cast(unsigned, b * 255.0f + 8388608.0f), yc = __builtin_bit_cast(unsigned, c * 255.0f + 8388608.0f), yd = __builtin_bit_cast(unsigned, d * 255.0f + 8388608.0f);
;     const unsigned w01 = __builtin_amdgcn_perm(yb, ya, 0x0c0c0400u), w23 = __builtin_amdgcn_perm(yd, yc, 0x0c0c0400u);
;     return __builtin_amdgcn_perm(w23, w01, 0x05040100u); }
;     __device__ __forceinline__ void operator()(AccRef acc, const GUnit& u, int wr, int wc, int fr, int fq) const {
;     ...
;             for (int m = 0; m < 4; ++m) { u32x4 w;
; #pragma unroll
;                 for (int bj = 0; bj < 2; ++bj)
; #pragma unroll
;                     for (int n = 0; n < 2; ++n) { const f32x4 v = acc[ai][bj][m][n]; w[bj * 2 + n] = pk4_u8(fsigmoid(v[0] * W8_INV), fsigmoid(v[1] * W8_INV), fsigmoid(v[2] * W8_INV), fsigmoid(v[3] * W8_INV)); }
;                 *(u32x4*)(base + (size_t)(ai * 128 + m * 16) * D) = w; }
	v_exp_f32_e32 v54, v54
	v_mul_f32_e32 v38, 0xbcb8aa3b, v38
	v_fmamk_f32 v86, v86, 0x437f0000, v196
	v_exp_f32_e32 v55, v55
	v_mul_f32_e32 v39, 0xbcb8aa3b, v39
	v_fmamk_f32 v87, v87, 0x437f0000, v196
	v_exp_f32_e32 v56, v56
	v_mul_f32_e32 v40, 0xbcb8aa3b, v40
	v_fmamk_f32 v88, v88, 0x437f0000, v196
	v_exp_f32_e32 v57, v57
	v_mul_f32_e32 v41, 0xbcb8aa3b, v41
	v_fmamk_f32 v89, v89, 0x437f0000, v196
	v_exp_f32_e32 v50, v50
	v_mul_f32_e32 v34, 0xbcb8aa3b, v34
	v_fmamk_f32 v82, v82, 0x437f0000, v196
	v_exp_f32_e32 v51, v51
	v_mul_f32_e32 v35, 0xbcb8aa3b, v35
	v_fmamk_f32 v83, v83, 0x437f0000, v196
	v_exp_f32_e32 v52, v52
	v_mul_f32_e32 v36, 0xbcb8aa3b, v36
	v_fmamk_f32 v84, v84, 0x437f0000, v196
	v_exp_f32_e32 v53, v53
	v_mul_f32_e32 v37, 0xbcb8aa3b, v37
	v_fmamk_f32 v85, v85, 0x437f0000, v196
	v_rcp_f32_e32 v78, v78
	v_add_f32_e32 v62, 1.0, v62
	v_perm_b32 v110, v111, v110, s67
	v_rcp_f32_e32 v79, v79
	v_add_f32_e32 v63, 1.0, v63
	v_perm_b32 v112, v113, v112, s67
	v_rcp_f32_e32 v80, v80
	v_add_f32_e32 v64, 1.0, v64
	v_perm_b32 v10, v112, v110, s68
	v_rcp_f32_e32 v81, v81
	v_add_f32_e32 v65, 1.0, v65
	v_perm_b32 v106, v107, v106, s67
	v_rcp_f32_e32 v74, v74
	v_add_f32_e32 v58, 1.0, v58
	v_perm_b32 v108, v109, v108, s67
	v_rcp_f32_e32 v75, v75
	v_add_f32_e32 v59, 1.0, v59
	v_perm_b32 v11, v108, v106, s68
	v_rcp_f32_e32 v76, v76
	v_add_f32_e32 v60, 1.0, v60
	v_perm_b32 v102, v103, v102, s67
	v_rcp_f32_e32 v77, v77
	v_add_f32_e32 v61, 1.0, v61
	v_perm_b32 v104, v105, v104, s67
	v_rcp_f32_e32 v70, v70
	v_add_f32_e32 v54, 1.0, v54
	v_perm_b32 v12, v104, v102, s68
	v_rcp_f32_e32 v71, v71
	v_add_f32_e32 v55, 1.0, v55
	v_perm_b32 v98, v99, v98, s67
	v_rcp_f32_e32 v72, v72
	v_add_f32_e32 v56, 1.0, v56
	v_perm_b32 v100, v101, v100, s67
	v_rcp_f32_e32 v73, v73
	v_add_f32_e32 v57, 1.0, v57
	v_perm_b32 v13, v100, v98, s68
	v_rcp_f32_e32 v66, v66
	v_add_f32_e32 v50, 1.0, v50
	v_add_co_u32_e32 v8, vcc, s62, v2
	v_rcp_f32_e32 v67, v67
	v_add_f32_e32 v51, 1.0, v51
	v_rcp_f32_e32 v68, v68
	v_add_f32_e32 v52, 1.0, v52
	v_addc_co_u32_e32 v9, vcc, 0, v3, vcc
	v_rcp_f32_e32 v69, v69
	v_add_f32_e32 v53, 1.0, v53
	global_store_dwordx4 v[8:9], v[10:13], off
	v_exp_f32_e32 v46, v46
	v_fmamk_f32 v78, v78, 0x437f0000, v196
	v_exp_f32_e32 v47, v47
	v_fmamk_f32 v79, v79, 0x437f0000, v196
	v_exp_f32_e32 v48, v48
	v_fmamk_f32 v80, v80, 0x437f0000, v196
	v_exp_f32_e32 v49, v49
	v_fmamk_f32 v81, v81, 0x437f0000, v196
	v_exp_f32_e32 v42, v42
	v_fmamk_f32 v74, v74, 0x437f0000, v196
	v_exp_f32_e32 v43, v43
	v_fmamk_f32 v75, v75, 0x437f0000, v196
	v_exp_f32_e32 v44, v44
	v_fmamk_f32 v76, v76, 0x437f0000, v196
	v_exp_f32_e32 v45, v45
	v_fmamk_f32 v77, v77, 0x437f0000, v196
	v_exp_f32_e32 v38, v38
	v_fmamk_f32 v70, v70, 0x437f0000, v196
	v_exp_f32_e32 v39, v39
	v_fmamk_f32 v71, v71, 0x437f0000, v196
	v_exp_f32_e32 v40, v40
	v_fmamk_f32 v72, v72, 0x437f0000, v196
	v_exp_f32_e32 v41, v41
	v_fmamk_f32 v73, v73, 0x437f0000, v196
	v_exp_f32_e32 v34, v34
	v_fmamk_f32 v66, v66, 0x437f0000, v196
	v_exp_f32_e32 v35, v35
	v_fmamk_f32 v67, v67, 0x437f0000, v196
	v_exp_f32_e32 v36, v36
	v_fmamk_f32 v68, v68, 0x437f0000, v196
	v_exp_f32_e32 v37, v37
	v_fmamk_f32 v69, v69, 0x437f0000, v196
	v_rcp_f32_e32 v62, v62
	v_add_f32_e32 v46, 1.0, v46
	v_perm_b32 v94, v95, v94, s67
	v_rcp_f32_e32 v63, v63
	v_add_f32_e32 v47, 1.0, v47
	v_perm_b32 v96, v97, v96, s67
	v_rcp_f32_e32 v64, v64
	v_add_f32_e32 v48, 1.0, v48
	v_perm_b32 v4, v96, v94, s68
	v_rcp_f32_e32 v65, v65
	v_add_f32_e32 v49, 1.0, v49
	v_perm_b32 v90, v91, v90, s67
	v_rcp_f32_e32 v58, v58
	v_add_f32_e32 v42, 1.0, v42
	v_perm_b32 v92, v93, v92, s67
	v_rcp_f32_e32 v59, v59
	v_add_f32_e32 v43, 1.0, v43
	v_perm_b32 v5, v92, v90, s68
	v_rcp_f32_e32 v60, v60
	v_add_f32_e32 v44, 1.0, v44
	v_perm_b32 v86, v87, v86, s67
	v_rcp_f32_e32 v61, v61
	v_add_f32_e32 v45, 1.0, v45
	v_perm_b32 v88, v89, v88, s67
	v_rcp_f32_e32 v54, v54
	v_add_f32_e32 v38, 1.0, v38
; __device__ __forceinline__ float fsigmoid(float x) { return __builtin_amdgcn_rcpf(1.0f + __builtin_amdgcn_exp2f(-1.44269504f * x)); }
; __device__ __forceinline__ unsigned pk4_u8(float a, float b, float c, float d) {
;     const unsigned ya = __builtin_bit_cast(unsigned, a * 255.0f + 8388608.0f), yb = __builtin_bit_cast(unsigned, b * 255.0f + 8388608.0f), yc = __builtin_bit_cast(unsigned, c * 255.0f + 8388608.0f), yd = __builtin_bit_cast(unsigned, d * 255.0f + 8388608.0f);
;     const unsigned w01 = __builtin_amdgcn_perm(yb, ya, 0x0c0c0400u), w23 = __builtin_amdgcn_perm(yd, yc, 0x0c0c0400u);
;     return __builtin_amdgcn_perm(w23, w01, 0x05040100u); }
;     __device__ __forceinline__ void operator()(AccRef acc, const GUnit& u, int wr, int wc, int fr, int fq) const {
;     ...
;             for (int m = 0; m < 4; ++m) { u32x4 w;
; #pragma unroll
;                 for (int bj = 0; bj < 2; ++bj)
; #pragma unroll
;                     for (int n = 0; n < 2; ++n) { const f32x4 v = acc[ai][bj][m][n]; w[bj * 2 + n] = pk4_u8(fsigmoid(v[0] * W8_INV), fsigmoid(v[1] * W8_INV), fsigmoid(v[2] * W8_INV), fsigmoid(v[3] * W8_INV)); }
;                 *(u32x4*)(base + (size_t)(ai * 128 + m * 16) * D) = w; }
	v_perm_b32 v6, v88, v86, s68
	v_rcp_f32_e32 v55, v55
	v_add_f32_e32 v39, 1.0, v39
	v_perm_b32 v82, v83, v82, s67
	v_rcp_f32_e32 v56, v56
	v_add_f32_e32 v40, 1.0, v40
	v_perm_b32 v84, v85, v84, s67
	v_rcp_f32_e32 v57, v57
	v_add_f32_e32 v41, 1.0, v41
	v_perm_b32 v7, v84, v82, s68
	v_rcp_f32_e32 v50, v50
	v_add_f32_e32 v34, 1.0, v34
	v_add_co_u32_e32 v8, vcc, s69, v2
	v_rcp_f32_e32 v51, v51
	v_add_f32_e32 v35, 1.0, v35
	v_rcp_f32_e32 v52, v52
	v_add_f32_e32 v36, 1.0, v36
	v_addc_co_u32_e32 v9, vcc, 0, v3, vcc
	v_rcp_f32_e32 v53, v53
	v_add_f32_e32 v37, 1.0, v37
	global_store_dwordx4 v[8:9], v[4:7], off
	v_fmamk_f32 v62, v62, 0x437f0000, v196
	v_fmamk_f32 v63, v63, 0x437f0000, v196
	v_fmamk_f32 v64, v64, 0x437f0000, v196
	v_fmamk_f32 v65, v65, 0x437f0000, v196
	v_fmamk_f32 v58, v58, 0x437f0000, v196
	v_fmamk_f32 v59, v59, 0x437f0000, v196
	v_fmamk_f32 v60, v60, 0x437f0000, v196
	v_fmamk_f32 v61, v61, 0x437f0000, v196
	v_fmamk_f32 v54, v54, 0x437f0000, v196
	v_fmamk_f32 v55, v55, 0x437f0000, v196
	v_fmamk_f32 v56, v56, 0x437f0000, v196
	v_fmamk_f32 v57, v57, 0x437f0000, v196
	v_fmamk_f32 v50, v50, 0x437f0000, v196
	v_fmamk_f32 v51, v51, 0x437f0000, v196
	v_fmamk_f32 v52, v52, 0x437f0000, v196
	v_fmamk_f32 v53, v53, 0x437f0000, v196
	v_rcp_f32_e32 v46, v46
	v_perm_b32 v78, v79, v78, s67
	v_rcp_f32_e32 v47, v47
	v_perm_b32 v80, v81, v80, s67
	v_rcp_f32_e32 v48, v48
	v_perm_b32 v10, v80, v78, s68
	v_rcp_f32_e32 v49, v49
	v_perm_b32 v74, v75, v74, s67
	v_rcp_f32_e32 v42, v42
	v_perm_b32 v76, v77, v76, s67
	v_rcp_f32_e32 v43, v43
	v_perm_b32 v11, v76, v74, s68
	v_rcp_f32_e32 v44, v44
	v_perm_b32 v70, v71, v70, s67
	v_rcp_f32_e32 v45, v45
	v_perm_b32 v72, v73, v72, s67
	v_rcp_f32_e32 v38, v38
	v_perm_b32 v12, v72, v70, s68
	v_rcp_f32_e32 v39, v39
	v_perm_b32 v66, v67, v66, s67
	v_rcp_f32_e32 v40, v40
	v_perm_b32 v68, v69, v68, s67
	v_rcp_f32_e32 v41, v41
	v_perm_b32 v13, v68, v66, s68
	v_rcp_f32_e32 v34, v34
	v_add_co_u32_e32 v8, vcc, s70, v2
	v_rcp_f32_e32 v35, v35
	v_rcp_f32_e32 v36, v36
	v_addc_co_u32_e32 v9, vcc, 0, v3, vcc
	v_rcp_f32_e32 v37, v37
	global_store_dwordx4 v[8:9], v[10:13], off
	v_fmamk_f32 v46, v46, 0x437f0000, v196
	v_fmamk_f32 v47, v47, 0x437f0000, v196
	v_fmamk_f32 v48, v48, 0x437f0000, v196
	v_fmamk_f32 v49, v49, 0x437f0000, v196
	v_fmamk_f32 v42, v42, 0x437f0000, v196
	v_fmamk_f32 v43, v43, 0x437f0000, v196
	v_fmamk_f32 v44, v44, 0x437f0000, v196
	v_fmamk_f32 v45, v45, 0x437f0000, v196
	v_fmamk_f32 v38, v38, 0x437f0000, v196
	v_fmamk_f32 v39, v39, 0x437f0000, v196
	v_fmamk_f32 v40, v40, 0x437f0000, v196
	v_fmamk_f32 v41, v41, 0x437f0000, v196
	v_fmamk_f32 v34, v34, 0x437f0000, v196
	v_fmamk_f32 v35, v35, 0x437f0000, v196
	v_fmamk_f32 v36, v36, 0x437f0000, v196
	v_fmamk_f32 v37, v37, 0x437f0000, v196
	v_perm_b32 v62, v63, v62, s67
	v_perm_b32 v64, v65, v64, s67
	v_perm_b32 v4, v64, v62, s68
	v_perm_b32 v58, v59, v58, s67
	v_perm_b32 v60, v61, v60, s67
	v_perm_b32 v5, v60, v58, s68
	v_perm_b32 v54, v55, v54, s67
	v_perm_b32 v56, v57, v56, s67
	v_perm_b32 v6, v56, v54, s68
	v_perm_b32 v50, v51, v50, s67
	v_perm_b32 v52, v53, v52, s67
	v_perm_b32 v7, v52, v50, s68
	v_add_co_u32_e32 v8, vcc, s71, v2
	s_nop 1
	v_addc_co_u32_e32 v9, vcc, 0, v3, vcc
	global_store_dwordx4 v[8:9], v[4:7], off
	v_perm_b32 v46, v47, v46, s67
	v_perm_b32 v48, v49, v48, s67
	v_perm_b32 v10, v48, v46, s68
	v_perm_b32 v42, v43, v42, s67
	v_perm_b32 v44, v45, v44, s67
	v_perm_b32 v11, v44, v42, s68
	v_perm_b32 v38, v39, v38, s67
	v_perm_b32 v40, v41, v40, s67
	v_perm_b32 v12, v40, v38, s68
	v_perm_b32 v34, v35, v34, s67
	v_perm_b32 v36, v37, v36, s67
	v_perm_b32 v13, v36, v34, s68
	v_add_co_u32_e32 v8, vcc, 0x58000, v2
	s_nop 1
	v_addc_co_u32_e32 v9, vcc, 0, v3, vcc
	global_store_dwordx4 v[8:9], v[10:13], off
	s_andn2_b64 vcc, exec, s[0:1]
	s_mov_b64 s[0:1], -1
	s_cbranch_vccnz .LBB0_420
	s_andn2_b64 vcc, exec, s[10:11]
	s_cbranch_vccnz .LBB0_419
	s_branch .LBB0_419
